# removed compiler-inserted vmcnt(0) waits in the gate-tile epilogue path (no loads feed it), on top of peel+kswz
# speedup vs baseline: 1.2482x; 1.0006x over previous
.LBB0_818:
	v_lshl_add_u32 v2, v208, 2, s90
	v_add_u32_e32 v241, 0xffffd400, v2
	v_add_u32_e32 v242, 0xffffd410, v2
	v_add_u32_e32 v243, 0xffffd600, v2
	v_add_u32_e32 v244, 0xffffd610, v2
	v_mov_b32_e32 v188, 0
	s_andn2_b64 vcc, exec, s[30:31]
	v_mov_b32_e32 v189, 0
	v_mov_b32_e32 v190, 0
	v_mov_b32_e32 v191, 0
	v_mov_b32_e32 v192, 0
	v_mov_b32_e32 v193, 0
	v_mov_b32_e32 v194, 0
	v_mov_b32_e32 v195, 0
	s_cbranch_vccnz .LBB0_820
	ds_read_b128 v[184:187], v241
	ds_read_b128 v[180:183], v242
	ds_read_b128 v[188:191], v243
	ds_read_b128 v[192:195], v244

.LBB0_824:
	v_mov_b32_e32 v172, 0
	s_andn2_b64 vcc, exec, s[30:31]
	v_mov_b32_e32 v173, 0
	v_mov_b32_e32 v174, 0
	v_mov_b32_e32 v175, 0
	v_mov_b32_e32 v176, 0
	v_mov_b32_e32 v177, 0
	v_mov_b32_e32 v178, 0
	v_mov_b32_e32 v179, 0
	s_cbranch_vccnz .LBB0_826
	ds_read_b128 v[168:171], v241
	ds_read_b128 v[164:167], v242
	ds_read_b128 v[172:175], v243
	ds_read_b128 v[176:179], v244

.LBB0_830:
	v_mov_b32_e32 v140, 0
	s_andn2_b64 vcc, exec, s[30:31]
	v_mov_b32_e32 v141, 0
	v_mov_b32_e32 v142, 0
	v_mov_b32_e32 v143, 0
	v_mov_b32_e32 v144, 0
	v_mov_b32_e32 v145, 0
	v_mov_b32_e32 v146, 0
	v_mov_b32_e32 v147, 0
	s_cbranch_vccnz .LBB0_832
	ds_read_b128 v[136:139], v241
	ds_read_b128 v[132:135], v242
	ds_read_b128 v[140:143], v243
	ds_read_b128 v[144:147], v244

.LBB0_836:
	v_mov_b32_e32 v108, 0
	s_andn2_b64 vcc, exec, s[30:31]
	v_mov_b32_e32 v109, 0
	v_mov_b32_e32 v110, 0
	v_mov_b32_e32 v111, 0
	v_mov_b32_e32 v112, 0
	v_mov_b32_e32 v113, 0
	v_mov_b32_e32 v114, 0
	v_mov_b32_e32 v115, 0
	s_cbranch_vccnz .LBB0_838
	ds_read_b128 v[104:107], v241
	ds_read_b128 v[100:103], v242
	ds_read_b128 v[108:111], v243
	ds_read_b128 v[112:115], v244

.LBB0_853:
	s_waitcnt lgkmcnt(0)
	v_add_f32_e32 v152, v152, v188
	v_add_f32_e32 v149, v149, v193
	v_mul_f32_e32 v152, 0xbfb8aa3b, v152
	v_add_f32_e32 v148, v148, v192
	v_mul_f32_e32 v149, 0xbfb8aa3b, v149
	v_exp_f32_e32 v152, v152
	v_mul_f32_e32 v148, 0xbfb8aa3b, v148
	v_exp_f32_e32 v149, v149
	v_exp_f32_e32 v148, v148
	v_add_f32_e32 v152, 1.0, v152
	v_add_f32_e32 v157, v157, v181
	v_add_f32_e32 v149, 1.0, v149
	v_rcp_f32_e32 v152, v152
	v_add_f32_e32 v148, 1.0, v148
	v_mul_f32_e32 v157, 0xbfb8aa3b, v157
	v_rcp_f32_e32 v149, v149
	v_rcp_f32_e32 v148, v148
	v_exp_f32_e32 v157, v157
	v_add_f32_e32 v160, v160, v184
	v_add_f32_e32 v156, v156, v180
	v_max_f32_e32 v180, 0xda24260, v152
	v_add_f32_e32 v152, v153, v189
	v_add_f32_e32 v153, v162, v186
	v_max_f32_e32 v184, 0xda24260, v149
	v_add_f32_e32 v149, v158, v182
	v_max_f32_e32 v181, 0xda24260, v148
	v_add_f32_e32 v148, 1.0, v157
	v_mul_f32_e32 v152, 0xbfb8aa3b, v152
	v_mul_f32_e32 v153, 0xbfb8aa3b, v153
	v_mul_f32_e32 v149, 0xbfb8aa3b, v149
	v_exp_f32_e32 v152, v152
	v_rcp_f32_e32 v148, v148
	v_exp_f32_e32 v153, v153
	v_exp_f32_e32 v149, v149
	v_add_f32_e32 v150, v150, v194
	v_add_f32_e32 v152, 1.0, v152
	v_max_f32_e32 v157, 0xda24260, v148
	v_add_f32_e32 v148, 1.0, v153
	v_add_f32_e32 v149, 1.0, v149
	v_mul_f32_e32 v150, 0xbfb8aa3b, v150
	v_rcp_f32_e32 v152, v152
	v_rcp_f32_e32 v148, v148
	v_rcp_f32_e32 v149, v149
	v_exp_f32_e32 v150, v150
	v_max_f32_e32 v162, 0xda24260, v152
	v_add_f32_e32 v152, v154, v190
	v_max_f32_e32 v154, 0xda24260, v148
	v_max_f32_e32 v158, 0xda24260, v149
	v_add_f32_e32 v148, 1.0, v150
	v_add_f32_e32 v149, v163, v187
	v_add_f32_e32 v150, v159, v183
	v_mul_f32_e32 v149, 0xbfb8aa3b, v149
	v_mul_f32_e32 v150, 0xbfb8aa3b, v150
	v_rcp_f32_e32 v148, v148
	v_exp_f32_e32 v149, v149
	v_exp_f32_e32 v150, v150
	v_add_f32_e32 v161, v161, v185
	v_mul_f32_e32 v160, 0xbfb8aa3b, v160
	v_mul_f32_e32 v161, 0xbfb8aa3b, v161
	v_exp_f32_e32 v160, v160
	v_exp_f32_e32 v161, v161
	v_mul_f32_e32 v152, 0xbfb8aa3b, v152
	v_max_f32_e32 v159, 0xda24260, v148
	v_add_f32_e32 v148, 1.0, v149
	v_add_f32_e32 v149, 1.0, v150
	v_exp_f32_e32 v152, v152
	v_rcp_f32_e32 v148, v148
	v_rcp_f32_e32 v149, v149
	s_add_i32 s19, s87, -11
	v_add_f32_e32 v160, 1.0, v160
	v_add_f32_e32 v161, 1.0, v161
	s_lshr_b32 s20, s19, 2
	v_rcp_f32_e32 v160, v160
	v_rcp_f32_e32 v161, v161
	v_add_f32_e32 v152, 1.0, v152
	v_add_f32_e32 v150, v155, v191
	v_max_f32_e32 v155, 0xda24260, v148
	v_max_f32_e32 v163, 0xda24260, v149
	v_mov_b32_e32 v148, s20
	v_mov_b32_e32 v149, v3
	v_rcp_f32_e32 v152, v152
	v_mad_i64_i32 v[148:149], s[20:21], v220, 3, v[148:149]
	v_lshlrev_b64 v[148:149], 10, v[148:149]
	s_lshl_b32 s19, s19, 8
	v_mul_f32_e32 v156, 0xbfb8aa3b, v156
	s_and_b32 s34, s19, 0x300
	v_lshl_add_u64 v[148:149], s[46:47], 0, v[148:149]
	v_exp_f32_e32 v156, v156
	v_max_f32_e32 v160, 0xda24260, v160
	v_max_f32_e32 v161, 0xda24260, v161
	v_lshl_add_u64 v[148:149], v[148:149], 0, s[34:35]
	v_max_f32_e32 v182, 0xda24260, v152
	v_lshl_add_u64 v[152:153], v[148:149], 0, v[2:3]
	v_add_u32_e32 v148, 0xc4820000, v160
	v_add_u32_e32 v149, 0xc4820000, v161
	v_ashrrev_i32_e32 v148, 18, v148
	v_ashrrev_i32_e32 v149, 18, v149
	v_med3_i32 v148, v148, 0, v236
	v_med3_i32 v149, v149, 0, v236
	v_add_f32_e32 v156, 1.0, v156
	v_rcp_f32_e32 v156, v156
	v_lshl_or_b32 v148, v149, 8, v148
	v_add_u32_e32 v149, 0xc4820000, v154
	v_add_u32_e32 v154, 0xc4820000, v155
	v_ashrrev_i32_e32 v149, 18, v149
	v_ashrrev_i32_e32 v154, 18, v154
	v_med3_i32 v149, v149, 0, v236
	v_med3_i32 v154, v154, 0, v236
	v_max_f32_e32 v156, 0xda24260, v156
	v_lshlrev_b32_e32 v149, 16, v149
	v_lshlrev_b32_e32 v154, 24, v154
	v_or3_b32 v148, v148, v149, v154
	v_add_u32_e32 v149, 0xc4820000, v156
	v_add_u32_e32 v154, 0xc4820000, v157
	v_ashrrev_i32_e32 v149, 18, v149
	v_ashrrev_i32_e32 v154, 18, v154
	v_mul_f32_e32 v150, 0xbfb8aa3b, v150
	v_med3_i32 v149, v149, 0, v236
	v_med3_i32 v154, v154, 0, v236
	v_exp_f32_e32 v150, v150
	v_add_u32_e32 v155, 0xc4820000, v163
	v_lshl_or_b32 v149, v154, 8, v149
	v_add_u32_e32 v154, 0xc4820000, v158
	v_ashrrev_i32_e32 v154, 18, v154
	v_ashrrev_i32_e32 v155, 18, v155
	v_med3_i32 v154, v154, 0, v236
	v_med3_i32 v155, v155, 0, v236
	v_add_f32_e32 v150, 1.0, v150
	v_rcp_f32_e32 v150, v150
	v_lshlrev_b32_e32 v154, 16, v154
	v_lshlrev_b32_e32 v155, 24, v155
	v_or3_b32 v149, v149, v154, v155
	v_add_u32_e32 v154, 0xc4820000, v180
	v_add_u32_e32 v155, 0xc4820000, v162
	v_add_f32_e32 v151, v151, v195
	v_ashrrev_i32_e32 v154, 18, v154
	v_ashrrev_i32_e32 v155, 18, v155
	v_mul_f32_e32 v151, 0xbfb8aa3b, v151
	v_med3_i32 v154, v154, 0, v236
	v_med3_i32 v155, v155, 0, v236
	v_exp_f32_e32 v151, v151
	v_max_f32_e32 v150, 0xda24260, v150
	v_add_u32_e32 v150, 0xc4820000, v150
	v_lshl_or_b32 v154, v155, 8, v154
	v_add_u32_e32 v155, 0xc4820000, v182
	v_ashrrev_i32_e32 v155, 18, v155
	v_ashrrev_i32_e32 v150, 18, v150
	v_med3_i32 v155, v155, 0, v236
	v_med3_i32 v150, v150, 0, v236
	v_add_f32_e32 v151, 1.0, v151
	v_rcp_f32_e32 v151, v151
	v_lshlrev_b32_e32 v155, 16, v155
	v_lshlrev_b32_e32 v150, 24, v150
	v_or3_b32 v150, v154, v155, v150
	v_add_u32_e32 v154, 0xc4820000, v181
	v_add_u32_e32 v155, 0xc4820000, v184
	v_ashrrev_i32_e32 v154, 18, v154
	v_ashrrev_i32_e32 v155, 18, v155
	v_med3_i32 v154, v154, 0, v236
	v_med3_i32 v155, v155, 0, v236
	v_max_f32_e32 v151, 0xda24260, v151
	v_add_u32_e32 v151, 0xc4820000, v151
	v_lshl_or_b32 v154, v155, 8, v154
	v_add_u32_e32 v155, 0xc4820000, v159
	v_ashrrev_i32_e32 v155, 18, v155
	v_ashrrev_i32_e32 v151, 18, v151
	v_med3_i32 v155, v155, 0, v236
	v_med3_i32 v151, v151, 0, v236
	v_mov_b32_e32 v223, 0
	v_lshlrev_b32_e32 v155, 16, v155
	v_lshlrev_b32_e32 v151, 24, v151
	v_or3_b32 v151, v154, v155, v151
	global_store_dwordx4 v[152:153], v[148:151], off
	s_and_b64 vcc, exec, s[40:41]
	s_mov_b64 s[26:27], -1
	s_cbranch_vccz .LBB0_925

.LBB0_855:
	s_waitcnt lgkmcnt(0)
	v_add_f32_e32 v120, v120, v172
	v_add_f32_e32 v117, v117, v177
	v_mul_f32_e32 v120, 0xbfb8aa3b, v120
	v_add_f32_e32 v116, v116, v176
	v_mul_f32_e32 v117, 0xbfb8aa3b, v117
	v_exp_f32_e32 v120, v120
	v_mul_f32_e32 v116, 0xbfb8aa3b, v116
	v_exp_f32_e32 v117, v117
	v_exp_f32_e32 v116, v116
	v_add_f32_e32 v120, 1.0, v120
	v_add_f32_e32 v125, v125, v165
	v_add_f32_e32 v117, 1.0, v117
	v_rcp_f32_e32 v120, v120
	v_add_f32_e32 v116, 1.0, v116
	v_mul_f32_e32 v125, 0xbfb8aa3b, v125
	v_rcp_f32_e32 v117, v117
	v_rcp_f32_e32 v116, v116
	v_exp_f32_e32 v125, v125
	v_max_f32_e32 v148, 0xda24260, v120
	v_add_f32_e32 v120, v121, v173
	v_add_f32_e32 v121, v130, v170
	v_max_f32_e32 v150, 0xda24260, v117
	v_add_f32_e32 v117, v126, v166
	v_max_f32_e32 v149, 0xda24260, v116
	v_add_f32_e32 v116, 1.0, v125
	v_mul_f32_e32 v120, 0xbfb8aa3b, v120
	v_mul_f32_e32 v121, 0xbfb8aa3b, v121
	v_mul_f32_e32 v117, 0xbfb8aa3b, v117
	v_exp_f32_e32 v120, v120
	v_rcp_f32_e32 v116, v116
	v_exp_f32_e32 v121, v121
	v_exp_f32_e32 v117, v117
	v_add_f32_e32 v118, v118, v178
	v_add_f32_e32 v120, 1.0, v120
	v_max_f32_e32 v125, 0xda24260, v116
	v_add_f32_e32 v116, 1.0, v121
	v_add_f32_e32 v117, 1.0, v117
	v_mul_f32_e32 v118, 0xbfb8aa3b, v118
	v_rcp_f32_e32 v120, v120
	v_rcp_f32_e32 v116, v116
	v_rcp_f32_e32 v117, v117
	v_exp_f32_e32 v118, v118
	v_max_f32_e32 v130, 0xda24260, v120
	v_add_f32_e32 v120, v122, v174
	v_max_f32_e32 v122, 0xda24260, v116
	v_max_f32_e32 v126, 0xda24260, v117
	v_add_f32_e32 v116, 1.0, v118
	v_add_f32_e32 v117, v131, v171
	v_add_f32_e32 v118, v127, v167
	v_mul_f32_e32 v117, 0xbfb8aa3b, v117
	v_mul_f32_e32 v118, 0xbfb8aa3b, v118
	v_rcp_f32_e32 v116, v116
	v_exp_f32_e32 v117, v117
	v_exp_f32_e32 v118, v118
	v_add_f32_e32 v128, v128, v168
	v_add_f32_e32 v129, v129, v169
	v_mul_f32_e32 v128, 0xbfb8aa3b, v128
	v_mul_f32_e32 v129, 0xbfb8aa3b, v129
	v_exp_f32_e32 v128, v128
	v_exp_f32_e32 v129, v129
	v_mul_f32_e32 v120, 0xbfb8aa3b, v120
	v_max_f32_e32 v127, 0xda24260, v116
	v_add_f32_e32 v116, 1.0, v117
	v_add_f32_e32 v117, 1.0, v118
	v_exp_f32_e32 v120, v120
	v_rcp_f32_e32 v116, v116
	v_rcp_f32_e32 v117, v117
	s_add_i32 s19, s87, -11
	v_add_f32_e32 v128, 1.0, v128
	v_add_f32_e32 v129, 1.0, v129
	s_lshr_b32 s20, s19, 2
	v_rcp_f32_e32 v128, v128
	v_rcp_f32_e32 v129, v129
	v_add_f32_e32 v120, 1.0, v120
	v_add_f32_e32 v118, v123, v175
	v_max_f32_e32 v123, 0xda24260, v116
	v_max_f32_e32 v131, 0xda24260, v117
	v_mov_b32_e32 v116, s20
	v_mov_b32_e32 v117, v3
	v_rcp_f32_e32 v120, v120
	v_mad_i64_i32 v[116:117], s[20:21], v226, 3, v[116:117]
	v_add_f32_e32 v124, v124, v164
	v_lshlrev_b64 v[116:117], 10, v[116:117]
	s_lshl_b32 s19, s19, 8
	v_mul_f32_e32 v124, 0xbfb8aa3b, v124
	s_and_b32 s34, s19, 0x300
	v_lshl_add_u64 v[116:117], s[46:47], 0, v[116:117]
	v_exp_f32_e32 v124, v124
	v_max_f32_e32 v128, 0xda24260, v128
	v_max_f32_e32 v129, 0xda24260, v129
	v_lshl_add_u64 v[116:117], v[116:117], 0, s[34:35]
	v_max_f32_e32 v151, 0xda24260, v120
	v_lshl_add_u64 v[120:121], v[116:117], 0, v[2:3]
	v_add_u32_e32 v116, 0xc4820000, v128
	v_add_u32_e32 v117, 0xc4820000, v129
	v_ashrrev_i32_e32 v116, 18, v116
	v_ashrrev_i32_e32 v117, 18, v117
	v_med3_i32 v116, v116, 0, v236
	v_med3_i32 v117, v117, 0, v236
	v_add_f32_e32 v124, 1.0, v124
	v_rcp_f32_e32 v124, v124
	v_lshl_or_b32 v116, v117, 8, v116
	v_add_u32_e32 v117, 0xc4820000, v122
	v_add_u32_e32 v122, 0xc4820000, v123
	v_ashrrev_i32_e32 v117, 18, v117
	v_ashrrev_i32_e32 v122, 18, v122
	v_med3_i32 v117, v117, 0, v236
	v_med3_i32 v122, v122, 0, v236
	v_max_f32_e32 v124, 0xda24260, v124
	v_lshlrev_b32_e32 v117, 16, v117
	v_lshlrev_b32_e32 v122, 24, v122
	v_or3_b32 v116, v116, v117, v122
	v_add_u32_e32 v117, 0xc4820000, v124
	v_add_u32_e32 v122, 0xc4820000, v125
	v_ashrrev_i32_e32 v117, 18, v117
	v_ashrrev_i32_e32 v122, 18, v122
	v_mul_f32_e32 v118, 0xbfb8aa3b, v118
	v_med3_i32 v117, v117, 0, v236
	v_med3_i32 v122, v122, 0, v236
	v_exp_f32_e32 v118, v118
	v_add_u32_e32 v123, 0xc4820000, v131
	v_lshl_or_b32 v117, v122, 8, v117
	v_add_u32_e32 v122, 0xc4820000, v126
	v_ashrrev_i32_e32 v122, 18, v122
	v_ashrrev_i32_e32 v123, 18, v123
	v_med3_i32 v122, v122, 0, v236
	v_med3_i32 v123, v123, 0, v236
	v_add_f32_e32 v118, 1.0, v118
	v_rcp_f32_e32 v118, v118
	v_lshlrev_b32_e32 v122, 16, v122
	v_lshlrev_b32_e32 v123, 24, v123
	v_or3_b32 v117, v117, v122, v123
	v_add_u32_e32 v122, 0xc4820000, v148
	v_add_u32_e32 v123, 0xc4820000, v130
	v_add_f32_e32 v119, v119, v179
	v_ashrrev_i32_e32 v122, 18, v122
	v_ashrrev_i32_e32 v123, 18, v123
	v_mul_f32_e32 v119, 0xbfb8aa3b, v119
	v_med3_i32 v122, v122, 0, v236
	v_med3_i32 v123, v123, 0, v236
	v_exp_f32_e32 v119, v119
	v_max_f32_e32 v118, 0xda24260, v118
	v_add_u32_e32 v118, 0xc4820000, v118
	v_lshl_or_b32 v122, v123, 8, v122
	v_add_u32_e32 v123, 0xc4820000, v151
	v_ashrrev_i32_e32 v123, 18, v123
	v_ashrrev_i32_e32 v118, 18, v118
	v_med3_i32 v123, v123, 0, v236
	v_med3_i32 v118, v118, 0, v236
	v_add_f32_e32 v119, 1.0, v119
	v_rcp_f32_e32 v119, v119
	v_lshlrev_b32_e32 v123, 16, v123
	v_lshlrev_b32_e32 v118, 24, v118
	v_or3_b32 v118, v122, v123, v118
	v_add_u32_e32 v122, 0xc4820000, v149
	v_add_u32_e32 v123, 0xc4820000, v150
	v_ashrrev_i32_e32 v122, 18, v122
	v_ashrrev_i32_e32 v123, 18, v123
	v_med3_i32 v122, v122, 0, v236
	v_med3_i32 v123, v123, 0, v236
	v_max_f32_e32 v119, 0xda24260, v119
	v_add_u32_e32 v119, 0xc4820000, v119
	v_lshl_or_b32 v122, v123, 8, v122
	v_add_u32_e32 v123, 0xc4820000, v127
	v_ashrrev_i32_e32 v123, 18, v123
	v_ashrrev_i32_e32 v119, 18, v119
	v_med3_i32 v123, v123, 0, v236
	v_med3_i32 v119, v119, 0, v236
	v_mov_b32_e32 v150, v223
	v_lshlrev_b32_e32 v123, 16, v123
	v_lshlrev_b32_e32 v119, 24, v119
	v_or3_b32 v119, v122, v123, v119
	global_store_dwordx4 v[120:121], v[116:119], off
	s_and_b64 vcc, exec, s[40:41]
	s_mov_b64 s[26:27], -1
	s_cbranch_vccz .LBB0_975

.LBB0_857:
	s_waitcnt lgkmcnt(0)
	v_add_f32_e32 v88, v88, v140
	v_add_f32_e32 v85, v85, v145
	v_mul_f32_e32 v88, 0xbfb8aa3b, v88
	v_add_f32_e32 v84, v84, v144
	v_mul_f32_e32 v85, 0xbfb8aa3b, v85
	v_exp_f32_e32 v88, v88
	v_mul_f32_e32 v84, 0xbfb8aa3b, v84
	v_exp_f32_e32 v85, v85
	v_exp_f32_e32 v84, v84
	v_add_f32_e32 v88, 1.0, v88
	v_add_f32_e32 v93, v93, v133
	v_add_f32_e32 v85, 1.0, v85
	v_rcp_f32_e32 v88, v88
	v_add_f32_e32 v84, 1.0, v84
	v_mul_f32_e32 v93, 0xbfb8aa3b, v93
	v_rcp_f32_e32 v85, v85
	v_rcp_f32_e32 v84, v84
	v_exp_f32_e32 v93, v93
	v_max_f32_e32 v116, 0xda24260, v88
	v_add_f32_e32 v88, v89, v141
	v_add_f32_e32 v89, v98, v138
	v_max_f32_e32 v118, 0xda24260, v85
	v_add_f32_e32 v85, v94, v134
	v_max_f32_e32 v117, 0xda24260, v84
	v_add_f32_e32 v84, 1.0, v93
	v_mul_f32_e32 v88, 0xbfb8aa3b, v88
	v_mul_f32_e32 v89, 0xbfb8aa3b, v89
	v_mul_f32_e32 v85, 0xbfb8aa3b, v85
	v_exp_f32_e32 v88, v88
	v_rcp_f32_e32 v84, v84
	v_exp_f32_e32 v89, v89
	v_exp_f32_e32 v85, v85
	v_add_f32_e32 v86, v86, v146
	v_add_f32_e32 v88, 1.0, v88
	v_max_f32_e32 v93, 0xda24260, v84
	v_add_f32_e32 v84, 1.0, v89
	v_add_f32_e32 v85, 1.0, v85
	v_mul_f32_e32 v86, 0xbfb8aa3b, v86
	v_rcp_f32_e32 v88, v88
	v_rcp_f32_e32 v84, v84
	v_rcp_f32_e32 v85, v85
	v_exp_f32_e32 v86, v86
	v_max_f32_e32 v98, 0xda24260, v88
	v_add_f32_e32 v88, v90, v142
	v_max_f32_e32 v90, 0xda24260, v84
	v_max_f32_e32 v94, 0xda24260, v85
	v_add_f32_e32 v84, 1.0, v86
	v_add_f32_e32 v85, v99, v139
	v_add_f32_e32 v86, v95, v135
	v_mul_f32_e32 v85, 0xbfb8aa3b, v85
	v_mul_f32_e32 v86, 0xbfb8aa3b, v86
	v_rcp_f32_e32 v84, v84
	v_exp_f32_e32 v85, v85
	v_exp_f32_e32 v86, v86
	v_add_f32_e32 v96, v96, v136
	v_add_f32_e32 v97, v97, v137
	v_mul_f32_e32 v96, 0xbfb8aa3b, v96
	v_mul_f32_e32 v97, 0xbfb8aa3b, v97
	v_exp_f32_e32 v96, v96
	v_exp_f32_e32 v97, v97
	v_mul_f32_e32 v88, 0xbfb8aa3b, v88
	v_max_f32_e32 v95, 0xda24260, v84
	v_add_f32_e32 v84, 1.0, v85
	v_add_f32_e32 v85, 1.0, v86
	v_exp_f32_e32 v88, v88
	v_rcp_f32_e32 v84, v84
	v_rcp_f32_e32 v85, v85
	s_add_i32 s19, s87, -11
	v_add_f32_e32 v96, 1.0, v96
	v_add_f32_e32 v97, 1.0, v97
	s_lshr_b32 s20, s19, 2
	v_rcp_f32_e32 v96, v96
	v_rcp_f32_e32 v97, v97
	v_add_f32_e32 v88, 1.0, v88
	v_add_f32_e32 v86, v91, v143
	v_max_f32_e32 v91, 0xda24260, v84
	v_max_f32_e32 v99, 0xda24260, v85
	v_mov_b32_e32 v84, s20
	v_mov_b32_e32 v85, v3
	v_rcp_f32_e32 v88, v88
	v_mad_i64_i32 v[84:85], s[20:21], v224, 3, v[84:85]
	v_add_f32_e32 v92, v92, v132
	v_lshlrev_b64 v[84:85], 10, v[84:85]
	s_lshl_b32 s19, s19, 8
	v_mul_f32_e32 v92, 0xbfb8aa3b, v92
	s_and_b32 s34, s19, 0x300
	v_lshl_add_u64 v[84:85], s[46:47], 0, v[84:85]
	v_exp_f32_e32 v92, v92
	v_max_f32_e32 v96, 0xda24260, v96
	v_max_f32_e32 v97, 0xda24260, v97
	v_lshl_add_u64 v[84:85], v[84:85], 0, s[34:35]
	v_max_f32_e32 v119, 0xda24260, v88
	v_lshl_add_u64 v[88:89], v[84:85], 0, v[2:3]
	v_add_u32_e32 v84, 0xc4820000, v96
	v_add_u32_e32 v85, 0xc4820000, v97
	v_ashrrev_i32_e32 v84, 18, v84
	v_ashrrev_i32_e32 v85, 18, v85
	v_med3_i32 v84, v84, 0, v236
	v_med3_i32 v85, v85, 0, v236
	v_add_f32_e32 v92, 1.0, v92
	v_rcp_f32_e32 v92, v92
	v_lshl_or_b32 v84, v85, 8, v84
	v_add_u32_e32 v85, 0xc4820000, v90
	v_add_u32_e32 v90, 0xc4820000, v91
	v_ashrrev_i32_e32 v85, 18, v85
	v_ashrrev_i32_e32 v90, 18, v90
	v_med3_i32 v85, v85, 0, v236
	v_med3_i32 v90, v90, 0, v236
	v_max_f32_e32 v92, 0xda24260, v92
	v_lshlrev_b32_e32 v85, 16, v85
	v_lshlrev_b32_e32 v90, 24, v90
	v_or3_b32 v84, v84, v85, v90
	v_add_u32_e32 v85, 0xc4820000, v92
	v_add_u32_e32 v90, 0xc4820000, v93
	v_ashrrev_i32_e32 v85, 18, v85
	v_ashrrev_i32_e32 v90, 18, v90
	v_mul_f32_e32 v86, 0xbfb8aa3b, v86
	v_med3_i32 v85, v85, 0, v236
	v_med3_i32 v90, v90, 0, v236
	v_exp_f32_e32 v86, v86
	v_add_u32_e32 v91, 0xc4820000, v99
	v_lshl_or_b32 v85, v90, 8, v85
	v_add_u32_e32 v90, 0xc4820000, v94
	v_ashrrev_i32_e32 v90, 18, v90
	v_ashrrev_i32_e32 v91, 18, v91
	v_med3_i32 v90, v90, 0, v236
	v_med3_i32 v91, v91, 0, v236
	v_add_f32_e32 v86, 1.0, v86
	v_rcp_f32_e32 v86, v86
	v_lshlrev_b32_e32 v90, 16, v90
	v_lshlrev_b32_e32 v91, 24, v91
	v_or3_b32 v85, v85, v90, v91
	v_add_u32_e32 v90, 0xc4820000, v116
	v_add_u32_e32 v91, 0xc4820000, v98
	v_add_f32_e32 v87, v87, v147
	v_ashrrev_i32_e32 v90, 18, v90
	v_ashrrev_i32_e32 v91, 18, v91
	v_mul_f32_e32 v87, 0xbfb8aa3b, v87
	v_med3_i32 v90, v90, 0, v236
	v_med3_i32 v91, v91, 0, v236
	v_exp_f32_e32 v87, v87
	v_max_f32_e32 v86, 0xda24260, v86
	v_add_u32_e32 v86, 0xc4820000, v86
	v_lshl_or_b32 v90, v91, 8, v90
	v_add_u32_e32 v91, 0xc4820000, v119
	v_ashrrev_i32_e32 v91, 18, v91
	v_ashrrev_i32_e32 v86, 18, v86
	v_med3_i32 v91, v91, 0, v236
	v_med3_i32 v86, v86, 0, v236
	v_add_f32_e32 v87, 1.0, v87
	v_rcp_f32_e32 v87, v87
	v_lshlrev_b32_e32 v91, 16, v91
	v_lshlrev_b32_e32 v86, 24, v86
	v_or3_b32 v86, v90, v91, v86
	v_add_u32_e32 v90, 0xc4820000, v117
	v_add_u32_e32 v91, 0xc4820000, v118
	v_ashrrev_i32_e32 v90, 18, v90
	v_ashrrev_i32_e32 v91, 18, v91
	v_med3_i32 v90, v90, 0, v236
	v_med3_i32 v91, v91, 0, v236
	v_max_f32_e32 v87, 0xda24260, v87
	v_add_u32_e32 v87, 0xc4820000, v87
	v_lshl_or_b32 v90, v91, 8, v90
	v_add_u32_e32 v91, 0xc4820000, v95
	v_ashrrev_i32_e32 v91, 18, v91
	v_ashrrev_i32_e32 v87, 18, v87
	v_med3_i32 v91, v91, 0, v236
	v_med3_i32 v87, v87, 0, v236
	v_mov_b32_e32 v118, v150
	v_lshlrev_b32_e32 v91, 16, v91
	v_lshlrev_b32_e32 v87, 24, v87
	v_or3_b32 v87, v90, v91, v87
	global_store_dwordx4 v[88:89], v[84:87], off
	s_and_b64 vcc, exec, s[40:41]
	s_mov_b64 s[26:27], -1
	s_cbranch_vccz .LBB0_1025

.LBB0_859:
	s_waitcnt lgkmcnt(0)
	v_add_f32_e32 v72, v72, v108
	v_add_f32_e32 v69, v69, v113
	v_mul_f32_e32 v72, 0xbfb8aa3b, v72
	v_add_f32_e32 v68, v68, v112
	v_mul_f32_e32 v69, 0xbfb8aa3b, v69
	v_exp_f32_e32 v72, v72
	v_mul_f32_e32 v68, 0xbfb8aa3b, v68
	v_exp_f32_e32 v69, v69
	v_exp_f32_e32 v68, v68
	v_add_f32_e32 v72, 1.0, v72
	v_add_f32_e32 v77, v77, v101
	v_add_f32_e32 v69, 1.0, v69
	v_rcp_f32_e32 v72, v72
	v_add_f32_e32 v68, 1.0, v68
	v_mul_f32_e32 v77, 0xbfb8aa3b, v77
	v_rcp_f32_e32 v69, v69
	v_rcp_f32_e32 v68, v68
	v_exp_f32_e32 v77, v77
	v_max_f32_e32 v84, 0xda24260, v72
	v_add_f32_e32 v72, v73, v109
	v_add_f32_e32 v73, v82, v106
	v_max_f32_e32 v86, 0xda24260, v69
	v_add_f32_e32 v69, v78, v102
	v_max_f32_e32 v85, 0xda24260, v68
	v_add_f32_e32 v68, 1.0, v77
	v_mul_f32_e32 v72, 0xbfb8aa3b, v72
	v_mul_f32_e32 v73, 0xbfb8aa3b, v73
	v_mul_f32_e32 v69, 0xbfb8aa3b, v69
	v_exp_f32_e32 v72, v72
	v_rcp_f32_e32 v68, v68
	v_exp_f32_e32 v73, v73
	v_exp_f32_e32 v69, v69
	v_add_f32_e32 v70, v70, v114
	v_add_f32_e32 v72, 1.0, v72
	v_max_f32_e32 v77, 0xda24260, v68
	v_add_f32_e32 v68, 1.0, v73
	v_add_f32_e32 v69, 1.0, v69
	v_mul_f32_e32 v70, 0xbfb8aa3b, v70
	v_rcp_f32_e32 v72, v72
	v_rcp_f32_e32 v68, v68
	v_rcp_f32_e32 v69, v69
	v_exp_f32_e32 v70, v70
	v_max_f32_e32 v82, 0xda24260, v72
	v_add_f32_e32 v72, v74, v110
	v_max_f32_e32 v74, 0xda24260, v68
	v_max_f32_e32 v78, 0xda24260, v69
	v_add_f32_e32 v68, 1.0, v70
	v_add_f32_e32 v69, v83, v107
	v_add_f32_e32 v70, v79, v103
	v_mul_f32_e32 v69, 0xbfb8aa3b, v69
	v_mul_f32_e32 v70, 0xbfb8aa3b, v70
	v_rcp_f32_e32 v68, v68
	v_exp_f32_e32 v69, v69
	v_exp_f32_e32 v70, v70
	v_add_f32_e32 v80, v80, v104
	v_add_f32_e32 v81, v81, v105
	v_mul_f32_e32 v80, 0xbfb8aa3b, v80
	v_mul_f32_e32 v81, 0xbfb8aa3b, v81
	v_exp_f32_e32 v80, v80
	v_exp_f32_e32 v81, v81
	v_mul_f32_e32 v72, 0xbfb8aa3b, v72
	v_max_f32_e32 v79, 0xda24260, v68
	v_add_f32_e32 v68, 1.0, v69
	v_add_f32_e32 v69, 1.0, v70
	v_exp_f32_e32 v72, v72
	v_rcp_f32_e32 v68, v68
	v_rcp_f32_e32 v69, v69
	s_add_i32 s19, s87, -11
	v_add_f32_e32 v80, 1.0, v80
	v_add_f32_e32 v81, 1.0, v81
	s_lshr_b32 s20, s19, 2
	v_rcp_f32_e32 v80, v80
	v_rcp_f32_e32 v81, v81
	v_add_f32_e32 v72, 1.0, v72
	v_add_f32_e32 v70, v75, v111
	v_max_f32_e32 v75, 0xda24260, v68
	v_max_f32_e32 v83, 0xda24260, v69
	v_mov_b32_e32 v68, s20
	v_mov_b32_e32 v69, v3
	v_rcp_f32_e32 v72, v72
	v_mad_i64_i32 v[68:69], s[20:21], v222, 3, v[68:69]
	v_add_f32_e32 v76, v76, v100
	v_lshlrev_b64 v[68:69], 10, v[68:69]
	s_lshl_b32 s19, s19, 8
	v_mul_f32_e32 v76, 0xbfb8aa3b, v76
	s_and_b32 s34, s19, 0x300
	v_lshl_add_u64 v[68:69], s[46:47], 0, v[68:69]
	v_exp_f32_e32 v76, v76
	v_max_f32_e32 v80, 0xda24260, v80
	v_max_f32_e32 v81, 0xda24260, v81
	v_lshl_add_u64 v[68:69], v[68:69], 0, s[34:35]
	v_max_f32_e32 v87, 0xda24260, v72
	v_lshl_add_u64 v[72:73], v[68:69], 0, v[2:3]
	v_add_u32_e32 v68, 0xc4820000, v80
	v_add_u32_e32 v69, 0xc4820000, v81
	v_ashrrev_i32_e32 v68, 18, v68
	v_ashrrev_i32_e32 v69, 18, v69
	v_med3_i32 v68, v68, 0, v236
	v_med3_i32 v69, v69, 0, v236
	v_add_f32_e32 v76, 1.0, v76
	v_rcp_f32_e32 v76, v76
	v_lshl_or_b32 v68, v69, 8, v68
	v_add_u32_e32 v69, 0xc4820000, v74
	v_add_u32_e32 v74, 0xc4820000, v75
	v_ashrrev_i32_e32 v69, 18, v69
	v_ashrrev_i32_e32 v74, 18, v74
	v_med3_i32 v69, v69, 0, v236
	v_med3_i32 v74, v74, 0, v236
	v_max_f32_e32 v76, 0xda24260, v76
	v_lshlrev_b32_e32 v69, 16, v69
	v_lshlrev_b32_e32 v74, 24, v74
	v_or3_b32 v68, v68, v69, v74
	v_add_u32_e32 v69, 0xc4820000, v76
	v_add_u32_e32 v74, 0xc4820000, v77
	v_ashrrev_i32_e32 v69, 18, v69
	v_ashrrev_i32_e32 v74, 18, v74
	v_mul_f32_e32 v70, 0xbfb8aa3b, v70
	v_med3_i32 v69, v69, 0, v236
	v_med3_i32 v74, v74, 0, v236
	v_exp_f32_e32 v70, v70
	v_add_u32_e32 v75, 0xc4820000, v83
	v_lshl_or_b32 v69, v74, 8, v69
	v_add_u32_e32 v74, 0xc4820000, v78
	v_ashrrev_i32_e32 v74, 18, v74
	v_ashrrev_i32_e32 v75, 18, v75
	v_med3_i32 v74, v74, 0, v236
	v_med3_i32 v75, v75, 0, v236
	v_add_f32_e32 v70, 1.0, v70
	v_rcp_f32_e32 v70, v70
	v_lshlrev_b32_e32 v74, 16, v74
	v_lshlrev_b32_e32 v75, 24, v75
	v_or3_b32 v69, v69, v74, v75
	v_add_u32_e32 v74, 0xc4820000, v84
	v_add_u32_e32 v75, 0xc4820000, v82
	v_add_f32_e32 v71, v71, v115
	v_ashrrev_i32_e32 v74, 18, v74
	v_ashrrev_i32_e32 v75, 18, v75
	v_mul_f32_e32 v71, 0xbfb8aa3b, v71
	v_med3_i32 v74, v74, 0, v236
	v_med3_i32 v75, v75, 0, v236
	v_exp_f32_e32 v71, v71
	v_max_f32_e32 v70, 0xda24260, v70
	v_add_u32_e32 v70, 0xc4820000, v70
	v_lshl_or_b32 v74, v75, 8, v74
	v_add_u32_e32 v75, 0xc4820000, v87
	v_ashrrev_i32_e32 v75, 18, v75
	v_ashrrev_i32_e32 v70, 18, v70
	v_med3_i32 v75, v75, 0, v236
	v_med3_i32 v70, v70, 0, v236
	v_add_f32_e32 v71, 1.0, v71
	v_rcp_f32_e32 v71, v71
	v_lshlrev_b32_e32 v75, 16, v75
	v_lshlrev_b32_e32 v70, 24, v70
	v_or3_b32 v70, v74, v75, v70
	v_add_u32_e32 v74, 0xc4820000, v85
	v_add_u32_e32 v75, 0xc4820000, v86
	v_ashrrev_i32_e32 v74, 18, v74
	v_ashrrev_i32_e32 v75, 18, v75
	v_med3_i32 v74, v74, 0, v236
	v_med3_i32 v75, v75, 0, v236
	v_max_f32_e32 v71, 0xda24260, v71
	v_add_u32_e32 v71, 0xc4820000, v71
	v_lshl_or_b32 v74, v75, 8, v74
	v_add_u32_e32 v75, 0xc4820000, v79
	v_ashrrev_i32_e32 v75, 18, v75
	v_ashrrev_i32_e32 v71, 18, v71
	v_med3_i32 v75, v75, 0, v236
	v_med3_i32 v71, v71, 0, v236
	v_mov_b32_e32 v142, v118
	v_lshlrev_b32_e32 v75, 16, v75
	v_lshlrev_b32_e32 v71, 24, v71
	v_or3_b32 v71, v74, v75, v71
	global_store_dwordx4 v[72:73], v[68:71], off

.LBB0_864:
	v_mov_b32_e32 v124, 0
	s_andn2_b64 vcc, exec, s[26:27]
	v_mov_b32_e32 v125, 0
	v_mov_b32_e32 v126, 0
	v_mov_b32_e32 v127, 0
	v_mov_b32_e32 v128, 0
	v_mov_b32_e32 v129, 0
	v_mov_b32_e32 v130, 0
	v_mov_b32_e32 v131, 0
	s_cbranch_vccnz .LBB0_866
	ds_read_b128 v[120:123], v241
	ds_read_b128 v[116:119], v242
	ds_read_b128 v[124:127], v243
	ds_read_b128 v[128:131], v244

.LBB0_870:
	v_mov_b32_e32 v108, 0
	s_andn2_b64 vcc, exec, s[26:27]
	v_mov_b32_e32 v109, 0
	v_mov_b32_e32 v110, 0
	v_mov_b32_e32 v111, 0
	v_mov_b32_e32 v112, 0
	v_mov_b32_e32 v113, 0
	v_mov_b32_e32 v114, 0
	v_mov_b32_e32 v115, 0
	s_cbranch_vccnz .LBB0_872
	ds_read_b128 v[104:107], v241
	ds_read_b128 v[100:103], v242
	ds_read_b128 v[108:111], v243
	ds_read_b128 v[112:115], v244

.LBB0_876:
	v_mov_b32_e32 v92, 0
	s_andn2_b64 vcc, exec, s[26:27]
	v_mov_b32_e32 v93, 0
	v_mov_b32_e32 v94, 0
	v_mov_b32_e32 v95, 0
	v_mov_b32_e32 v96, 0
	v_mov_b32_e32 v97, 0
	v_mov_b32_e32 v98, 0
	v_mov_b32_e32 v99, 0
	s_cbranch_vccnz .LBB0_878
	ds_read_b128 v[88:91], v241
	ds_read_b128 v[84:87], v242
	ds_read_b128 v[92:95], v243
	ds_read_b128 v[96:99], v244

.LBB0_882:
	v_mov_b32_e32 v76, 0
	s_andn2_b64 vcc, exec, s[26:27]
	v_mov_b32_e32 v77, 0
	v_mov_b32_e32 v78, 0
	v_mov_b32_e32 v79, 0
	v_mov_b32_e32 v80, 0
	v_mov_b32_e32 v81, 0
	v_mov_b32_e32 v82, 0
	v_mov_b32_e32 v83, 0
	s_cbranch_vccnz .LBB0_899
	ds_read_b128 v[72:75], v241
	ds_read_b128 v[68:71], v242
	ds_read_b128 v[76:79], v243
	ds_read_b128 v[80:83], v244
	s_and_b64 vcc, exec, s[40:41]
	s_mov_b64 s[26:27], -1
	s_cbranch_vccz .LBB0_900

.LBB0_885:
	s_waitcnt lgkmcnt(1)
	v_add_f32_e32 v56, v56, v124
	s_waitcnt lgkmcnt(0)
	v_add_f32_e32 v53, v53, v129
	v_mul_f32_e32 v56, 0xbfb8aa3b, v56
	v_add_f32_e32 v52, v52, v128
	v_mul_f32_e32 v53, 0xbfb8aa3b, v53
	v_exp_f32_e32 v56, v56
	v_mul_f32_e32 v52, 0xbfb8aa3b, v52
	v_exp_f32_e32 v53, v53
	v_exp_f32_e32 v52, v52
	v_add_f32_e32 v56, 1.0, v56
	v_add_f32_e32 v61, v61, v117
	v_add_f32_e32 v53, 1.0, v53
	v_rcp_f32_e32 v56, v56
	v_add_f32_e32 v52, 1.0, v52
	v_mul_f32_e32 v61, 0xbfb8aa3b, v61
	v_rcp_f32_e32 v53, v53
	v_rcp_f32_e32 v52, v52
	v_exp_f32_e32 v61, v61
	v_add_f32_e32 v64, v64, v120
	v_add_f32_e32 v60, v60, v116
	v_max_f32_e32 v116, 0xda24260, v56
	v_add_f32_e32 v56, v57, v125
	v_add_f32_e32 v57, v66, v122
	v_max_f32_e32 v120, 0xda24260, v53
	v_add_f32_e32 v53, v62, v118
	v_max_f32_e32 v117, 0xda24260, v52
	v_add_f32_e32 v52, 1.0, v61
	v_mul_f32_e32 v56, 0xbfb8aa3b, v56
	v_mul_f32_e32 v57, 0xbfb8aa3b, v57
	v_mul_f32_e32 v53, 0xbfb8aa3b, v53
	v_exp_f32_e32 v56, v56
	v_rcp_f32_e32 v52, v52
	v_exp_f32_e32 v57, v57
	v_exp_f32_e32 v53, v53
	v_add_f32_e32 v54, v54, v130
	v_add_f32_e32 v56, 1.0, v56
	v_max_f32_e32 v61, 0xda24260, v52
	v_add_f32_e32 v52, 1.0, v57
	v_add_f32_e32 v53, 1.0, v53
	v_mul_f32_e32 v54, 0xbfb8aa3b, v54
	v_rcp_f32_e32 v56, v56
	v_rcp_f32_e32 v52, v52
	v_rcp_f32_e32 v53, v53
	v_exp_f32_e32 v54, v54
	v_max_f32_e32 v66, 0xda24260, v56
	v_add_f32_e32 v56, v58, v126
	v_max_f32_e32 v58, 0xda24260, v52
	v_max_f32_e32 v62, 0xda24260, v53
	v_add_f32_e32 v52, 1.0, v54
	v_add_f32_e32 v53, v67, v123
	v_add_f32_e32 v54, v63, v119
	v_mul_f32_e32 v53, 0xbfb8aa3b, v53
	v_mul_f32_e32 v54, 0xbfb8aa3b, v54
	v_rcp_f32_e32 v52, v52
	v_exp_f32_e32 v53, v53
	v_exp_f32_e32 v54, v54
	v_add_f32_e32 v65, v65, v121
	v_mul_f32_e32 v64, 0xbfb8aa3b, v64
	v_mul_f32_e32 v65, 0xbfb8aa3b, v65
	v_exp_f32_e32 v64, v64
	v_exp_f32_e32 v65, v65
	v_mul_f32_e32 v56, 0xbfb8aa3b, v56
	v_max_f32_e32 v63, 0xda24260, v52
	v_add_f32_e32 v52, 1.0, v53
	v_add_f32_e32 v53, 1.0, v54
	v_exp_f32_e32 v56, v56
	v_rcp_f32_e32 v52, v52
	v_rcp_f32_e32 v53, v53
	s_add_i32 s19, s87, -11
	v_add_f32_e32 v64, 1.0, v64
	v_add_f32_e32 v65, 1.0, v65
	s_lshr_b32 s20, s19, 2
	v_rcp_f32_e32 v64, v64
	v_rcp_f32_e32 v65, v65
	v_add_f32_e32 v56, 1.0, v56
	v_add_f32_e32 v54, v59, v127
	v_max_f32_e32 v59, 0xda24260, v52
	v_max_f32_e32 v67, 0xda24260, v53
	v_mov_b32_e32 v52, s20
	v_mov_b32_e32 v53, v3
	v_rcp_f32_e32 v56, v56
	v_mad_i64_i32 v[52:53], s[20:21], v138, 3, v[52:53]
	v_lshlrev_b64 v[52:53], 10, v[52:53]
	s_lshl_b32 s19, s19, 8
	v_mul_f32_e32 v60, 0xbfb8aa3b, v60
	s_and_b32 s34, s19, 0x300
	v_lshl_add_u64 v[52:53], s[46:47], 0, v[52:53]
	v_exp_f32_e32 v60, v60
	v_max_f32_e32 v64, 0xda24260, v64
	v_max_f32_e32 v65, 0xda24260, v65
	v_lshl_add_u64 v[52:53], v[52:53], 0, s[34:35]
	v_max_f32_e32 v118, 0xda24260, v56
	v_lshl_add_u64 v[56:57], v[52:53], 0, v[2:3]
	v_add_u32_e32 v52, 0xc4820000, v64
	v_add_u32_e32 v53, 0xc4820000, v65
	v_ashrrev_i32_e32 v52, 18, v52
	v_ashrrev_i32_e32 v53, 18, v53
	v_med3_i32 v52, v52, 0, v236
	v_med3_i32 v53, v53, 0, v236
	v_add_f32_e32 v60, 1.0, v60
	v_rcp_f32_e32 v60, v60
	v_lshl_or_b32 v52, v53, 8, v52
	v_add_u32_e32 v53, 0xc4820000, v58
	v_add_u32_e32 v58, 0xc4820000, v59
	v_ashrrev_i32_e32 v53, 18, v53
	v_ashrrev_i32_e32 v58, 18, v58
	v_med3_i32 v53, v53, 0, v236
	v_med3_i32 v58, v58, 0, v236
	v_max_f32_e32 v60, 0xda24260, v60
	v_lshlrev_b32_e32 v53, 16, v53
	v_lshlrev_b32_e32 v58, 24, v58
	v_or3_b32 v52, v52, v53, v58
	v_add_u32_e32 v53, 0xc4820000, v60
	v_add_u32_e32 v58, 0xc4820000, v61
	v_ashrrev_i32_e32 v53, 18, v53
	v_ashrrev_i32_e32 v58, 18, v58
	v_mul_f32_e32 v54, 0xbfb8aa3b, v54
	v_med3_i32 v53, v53, 0, v236
	v_med3_i32 v58, v58, 0, v236
	v_exp_f32_e32 v54, v54
	v_add_u32_e32 v59, 0xc4820000, v67
	v_lshl_or_b32 v53, v58, 8, v53
	v_add_u32_e32 v58, 0xc4820000, v62
	v_ashrrev_i32_e32 v58, 18, v58
	v_ashrrev_i32_e32 v59, 18, v59
	v_med3_i32 v58, v58, 0, v236
	v_med3_i32 v59, v59, 0, v236
	v_add_f32_e32 v54, 1.0, v54
	v_rcp_f32_e32 v54, v54
	v_lshlrev_b32_e32 v58, 16, v58
	v_lshlrev_b32_e32 v59, 24, v59
	v_or3_b32 v53, v53, v58, v59
	v_add_u32_e32 v58, 0xc4820000, v116
	v_add_u32_e32 v59, 0xc4820000, v66
	v_add_f32_e32 v55, v55, v131
	v_ashrrev_i32_e32 v58, 18, v58
	v_ashrrev_i32_e32 v59, 18, v59
	v_mul_f32_e32 v55, 0xbfb8aa3b, v55
	v_med3_i32 v58, v58, 0, v236
	v_med3_i32 v59, v59, 0, v236
	v_exp_f32_e32 v55, v55
	v_max_f32_e32 v54, 0xda24260, v54
	v_add_u32_e32 v54, 0xc4820000, v54
	v_lshl_or_b32 v58, v59, 8, v58
	v_add_u32_e32 v59, 0xc4820000, v118
	v_ashrrev_i32_e32 v59, 18, v59
	v_ashrrev_i32_e32 v54, 18, v54
	v_med3_i32 v59, v59, 0, v236
	v_med3_i32 v54, v54, 0, v236
	v_add_f32_e32 v55, 1.0, v55
	v_rcp_f32_e32 v55, v55
	v_lshlrev_b32_e32 v59, 16, v59
	v_lshlrev_b32_e32 v54, 24, v54
	v_or3_b32 v54, v58, v59, v54
	v_add_u32_e32 v58, 0xc4820000, v117
	v_add_u32_e32 v59, 0xc4820000, v120
	v_ashrrev_i32_e32 v58, 18, v58
	v_ashrrev_i32_e32 v59, 18, v59
	v_med3_i32 v58, v58, 0, v236
	v_med3_i32 v59, v59, 0, v236
	v_max_f32_e32 v55, 0xda24260, v55
	v_add_u32_e32 v55, 0xc4820000, v55
	v_lshl_or_b32 v58, v59, 8, v58
	v_add_u32_e32 v59, 0xc4820000, v63
	v_ashrrev_i32_e32 v59, 18, v59
	v_ashrrev_i32_e32 v55, 18, v55
	v_med3_i32 v59, v59, 0, v236
	v_med3_i32 v55, v55, 0, v236
	v_mov_b32_e32 v133, v142
	v_lshlrev_b32_e32 v59, 16, v59
	v_lshlrev_b32_e32 v55, 24, v55
	v_or3_b32 v55, v58, v59, v55
	global_store_dwordx4 v[56:57], v[52:55], off
	s_and_b64 vcc, exec, s[40:41]
	s_mov_b64 s[26:27], -1
	s_cbranch_vccz .LBB0_950

.LBB0_887:
	s_waitcnt lgkmcnt(1)
	v_add_f32_e32 v40, v40, v108
	s_waitcnt lgkmcnt(0)
	v_add_f32_e32 v37, v37, v113
	v_mul_f32_e32 v40, 0xbfb8aa3b, v40
	v_add_f32_e32 v36, v36, v112
	v_mul_f32_e32 v37, 0xbfb8aa3b, v37
	v_exp_f32_e32 v40, v40
	v_mul_f32_e32 v36, 0xbfb8aa3b, v36
	v_exp_f32_e32 v37, v37
	v_exp_f32_e32 v36, v36
	v_add_f32_e32 v40, 1.0, v40
	v_add_f32_e32 v45, v45, v101
	v_add_f32_e32 v37, 1.0, v37
	v_rcp_f32_e32 v40, v40
	v_add_f32_e32 v36, 1.0, v36
	v_mul_f32_e32 v45, 0xbfb8aa3b, v45
	v_rcp_f32_e32 v37, v37
	v_rcp_f32_e32 v36, v36
	v_exp_f32_e32 v45, v45
	v_max_f32_e32 v52, 0xda24260, v40
	v_add_f32_e32 v40, v41, v109
	v_add_f32_e32 v41, v50, v106
	v_max_f32_e32 v54, 0xda24260, v37
	v_add_f32_e32 v37, v46, v102
	v_max_f32_e32 v53, 0xda24260, v36
	v_add_f32_e32 v36, 1.0, v45
	v_mul_f32_e32 v40, 0xbfb8aa3b, v40
	v_mul_f32_e32 v41, 0xbfb8aa3b, v41
	v_mul_f32_e32 v37, 0xbfb8aa3b, v37
	v_exp_f32_e32 v40, v40
	v_rcp_f32_e32 v36, v36
	v_exp_f32_e32 v41, v41
	v_exp_f32_e32 v37, v37
	v_add_f32_e32 v38, v38, v114
	v_add_f32_e32 v40, 1.0, v40
	v_max_f32_e32 v45, 0xda24260, v36
	v_add_f32_e32 v36, 1.0, v41
	v_add_f32_e32 v37, 1.0, v37
	v_mul_f32_e32 v38, 0xbfb8aa3b, v38
	v_rcp_f32_e32 v40, v40
	v_rcp_f32_e32 v36, v36
	v_rcp_f32_e32 v37, v37
	v_exp_f32_e32 v38, v38
	v_max_f32_e32 v50, 0xda24260, v40
	v_add_f32_e32 v40, v42, v110
	v_max_f32_e32 v42, 0xda24260, v36
	v_max_f32_e32 v46, 0xda24260, v37
	v_add_f32_e32 v36, 1.0, v38
	v_add_f32_e32 v37, v51, v107
	v_add_f32_e32 v38, v47, v103
	v_mul_f32_e32 v37, 0xbfb8aa3b, v37
	v_mul_f32_e32 v38, 0xbfb8aa3b, v38
	v_rcp_f32_e32 v36, v36
	v_exp_f32_e32 v37, v37
	v_exp_f32_e32 v38, v38
	v_add_f32_e32 v48, v48, v104
	v_add_f32_e32 v49, v49, v105
	v_mul_f32_e32 v48, 0xbfb8aa3b, v48
	v_mul_f32_e32 v49, 0xbfb8aa3b, v49
	v_exp_f32_e32 v48, v48
	v_exp_f32_e32 v49, v49
	v_mul_f32_e32 v40, 0xbfb8aa3b, v40
	v_max_f32_e32 v47, 0xda24260, v36
	v_add_f32_e32 v36, 1.0, v37
	v_add_f32_e32 v37, 1.0, v38
	v_exp_f32_e32 v40, v40
	v_rcp_f32_e32 v36, v36
	v_rcp_f32_e32 v37, v37
	s_add_i32 s19, s87, -11
	v_add_f32_e32 v48, 1.0, v48
	v_add_f32_e32 v49, 1.0, v49
	s_lshr_b32 s20, s19, 2
	v_rcp_f32_e32 v48, v48
	v_rcp_f32_e32 v49, v49
	v_add_f32_e32 v40, 1.0, v40
	v_add_f32_e32 v38, v43, v111
	v_max_f32_e32 v43, 0xda24260, v36
	v_max_f32_e32 v51, 0xda24260, v37
	v_mov_b32_e32 v36, s20
	v_mov_b32_e32 v37, v3
	v_rcp_f32_e32 v40, v40
	v_mad_i64_i32 v[36:37], s[20:21], v136, 3, v[36:37]
	v_add_f32_e32 v44, v44, v100
	v_lshlrev_b64 v[36:37], 10, v[36:37]
	s_lshl_b32 s19, s19, 8
	v_mul_f32_e32 v44, 0xbfb8aa3b, v44
	s_and_b32 s34, s19, 0x300
	v_lshl_add_u64 v[36:37], s[46:47], 0, v[36:37]
	v_exp_f32_e32 v44, v44
	v_max_f32_e32 v48, 0xda24260, v48
	v_max_f32_e32 v49, 0xda24260, v49
	v_lshl_add_u64 v[36:37], v[36:37], 0, s[34:35]
	v_max_f32_e32 v55, 0xda24260, v40
	v_lshl_add_u64 v[40:41], v[36:37], 0, v[2:3]
	v_add_u32_e32 v36, 0xc4820000, v48
	v_add_u32_e32 v37, 0xc4820000, v49
	v_ashrrev_i32_e32 v36, 18, v36
	v_ashrrev_i32_e32 v37, 18, v37
	v_med3_i32 v36, v36, 0, v236
	v_med3_i32 v37, v37, 0, v236
	v_add_f32_e32 v44, 1.0, v44
	v_rcp_f32_e32 v44, v44
	v_lshl_or_b32 v36, v37, 8, v36
	v_add_u32_e32 v37, 0xc4820000, v42
	v_add_u32_e32 v42, 0xc4820000, v43
	v_ashrrev_i32_e32 v37, 18, v37
	v_ashrrev_i32_e32 v42, 18, v42
	v_med3_i32 v37, v37, 0, v236
	v_med3_i32 v42, v42, 0, v236
	v_max_f32_e32 v44, 0xda24260, v44
	v_lshlrev_b32_e32 v37, 16, v37
	v_lshlrev_b32_e32 v42, 24, v42
	v_or3_b32 v36, v36, v37, v42
	v_add_u32_e32 v37, 0xc4820000, v44
	v_add_u32_e32 v42, 0xc4820000, v45
	v_ashrrev_i32_e32 v37, 18, v37
	v_ashrrev_i32_e32 v42, 18, v42
	v_mul_f32_e32 v38, 0xbfb8aa3b, v38
	v_med3_i32 v37, v37, 0, v236
	v_med3_i32 v42, v42, 0, v236
	v_exp_f32_e32 v38, v38
	v_add_u32_e32 v43, 0xc4820000, v51
	v_lshl_or_b32 v37, v42, 8, v37
	v_add_u32_e32 v42, 0xc4820000, v46
	v_ashrrev_i32_e32 v42, 18, v42
	v_ashrrev_i32_e32 v43, 18, v43
	v_med3_i32 v42, v42, 0, v236
	v_med3_i32 v43, v43, 0, v236
	v_add_f32_e32 v38, 1.0, v38
	v_rcp_f32_e32 v38, v38
	v_lshlrev_b32_e32 v42, 16, v42
	v_lshlrev_b32_e32 v43, 24, v43
	v_or3_b32 v37, v37, v42, v43
	v_add_u32_e32 v42, 0xc4820000, v52
	v_add_u32_e32 v43, 0xc4820000, v50
	v_add_f32_e32 v39, v39, v115
	v_ashrrev_i32_e32 v42, 18, v42
	v_ashrrev_i32_e32 v43, 18, v43
	v_mul_f32_e32 v39, 0xbfb8aa3b, v39
	v_med3_i32 v42, v42, 0, v236
	v_med3_i32 v43, v43, 0, v236
	v_exp_f32_e32 v39, v39
	v_max_f32_e32 v38, 0xda24260, v38
	v_add_u32_e32 v38, 0xc4820000, v38
	v_lshl_or_b32 v42, v43, 8, v42
	v_add_u32_e32 v43, 0xc4820000, v55
	v_ashrrev_i32_e32 v43, 18, v43
	v_ashrrev_i32_e32 v38, 18, v38
	v_med3_i32 v43, v43, 0, v236
	v_med3_i32 v38, v38, 0, v236
	v_add_f32_e32 v39, 1.0, v39
	v_rcp_f32_e32 v39, v39
	v_lshlrev_b32_e32 v43, 16, v43
	v_lshlrev_b32_e32 v38, 24, v38
	v_or3_b32 v38, v42, v43, v38
	v_add_u32_e32 v42, 0xc4820000, v53
	v_add_u32_e32 v43, 0xc4820000, v54
	v_ashrrev_i32_e32 v42, 18, v42
	v_ashrrev_i32_e32 v43, 18, v43
	v_med3_i32 v42, v42, 0, v236
	v_med3_i32 v43, v43, 0, v236
	v_max_f32_e32 v39, 0xda24260, v39
	v_add_u32_e32 v39, 0xc4820000, v39
	v_lshl_or_b32 v42, v43, 8, v42
	v_add_u32_e32 v43, 0xc4820000, v47
	v_ashrrev_i32_e32 v43, 18, v43
	v_ashrrev_i32_e32 v39, 18, v39
	v_med3_i32 v43, v43, 0, v236
	v_med3_i32 v39, v39, 0, v236
	v_mov_b32_e32 v54, v133
	v_lshlrev_b32_e32 v43, 16, v43
	v_lshlrev_b32_e32 v39, 24, v39
	v_or3_b32 v39, v42, v43, v39
	global_store_dwordx4 v[40:41], v[36:39], off
	s_and_b64 vcc, exec, s[40:41]
	s_mov_b64 s[26:27], -1
	s_cbranch_vccz .LBB0_1000

.LBB0_889:
	s_waitcnt lgkmcnt(1)
	v_add_f32_e32 v24, v24, v92
	s_waitcnt lgkmcnt(0)
	v_add_f32_e32 v21, v21, v97
	v_mul_f32_e32 v24, 0xbfb8aa3b, v24
	v_add_f32_e32 v20, v20, v96
	v_mul_f32_e32 v21, 0xbfb8aa3b, v21
	v_exp_f32_e32 v24, v24
	v_mul_f32_e32 v20, 0xbfb8aa3b, v20
	v_exp_f32_e32 v21, v21
	v_exp_f32_e32 v20, v20
	v_add_f32_e32 v24, 1.0, v24
	v_add_f32_e32 v29, v29, v85
	v_add_f32_e32 v21, 1.0, v21
	v_rcp_f32_e32 v24, v24
	v_add_f32_e32 v20, 1.0, v20
	v_mul_f32_e32 v29, 0xbfb8aa3b, v29
	v_rcp_f32_e32 v21, v21
	v_rcp_f32_e32 v20, v20
	v_exp_f32_e32 v29, v29
	v_max_f32_e32 v36, 0xda24260, v24
	v_add_f32_e32 v24, v25, v93
	v_add_f32_e32 v25, v34, v90
	v_max_f32_e32 v38, 0xda24260, v21
	v_add_f32_e32 v21, v30, v86
	v_max_f32_e32 v37, 0xda24260, v20
	v_add_f32_e32 v20, 1.0, v29
	v_mul_f32_e32 v24, 0xbfb8aa3b, v24
	v_mul_f32_e32 v25, 0xbfb8aa3b, v25
	v_mul_f32_e32 v21, 0xbfb8aa3b, v21
	v_exp_f32_e32 v24, v24
	v_rcp_f32_e32 v20, v20
	v_exp_f32_e32 v25, v25
	v_exp_f32_e32 v21, v21
	v_add_f32_e32 v22, v22, v98
	v_add_f32_e32 v24, 1.0, v24
	v_max_f32_e32 v29, 0xda24260, v20
	v_add_f32_e32 v20, 1.0, v25
	v_add_f32_e32 v21, 1.0, v21
	v_mul_f32_e32 v22, 0xbfb8aa3b, v22
	v_rcp_f32_e32 v24, v24
	v_rcp_f32_e32 v20, v20
	v_rcp_f32_e32 v21, v21
	v_exp_f32_e32 v22, v22
	v_max_f32_e32 v34, 0xda24260, v24
	v_add_f32_e32 v24, v26, v94
	v_max_f32_e32 v26, 0xda24260, v20
	v_max_f32_e32 v30, 0xda24260, v21
	v_add_f32_e32 v20, 1.0, v22
	v_add_f32_e32 v21, v35, v91
	v_add_f32_e32 v22, v31, v87
	v_mul_f32_e32 v21, 0xbfb8aa3b, v21
	v_mul_f32_e32 v22, 0xbfb8aa3b, v22
	v_rcp_f32_e32 v20, v20
	v_exp_f32_e32 v21, v21
	v_exp_f32_e32 v22, v22
	v_add_f32_e32 v32, v32, v88
	v_add_f32_e32 v33, v33, v89
	v_mul_f32_e32 v32, 0xbfb8aa3b, v32
	v_mul_f32_e32 v33, 0xbfb8aa3b, v33
	v_exp_f32_e32 v32, v32
	v_exp_f32_e32 v33, v33
	v_mul_f32_e32 v24, 0xbfb8aa3b, v24
	v_max_f32_e32 v31, 0xda24260, v20
	v_add_f32_e32 v20, 1.0, v21
	v_add_f32_e32 v21, 1.0, v22
	v_exp_f32_e32 v24, v24
	v_rcp_f32_e32 v20, v20
	v_rcp_f32_e32 v21, v21
	s_add_i32 s19, s87, -11
	v_add_f32_e32 v32, 1.0, v32
	v_add_f32_e32 v33, 1.0, v33
	s_lshr_b32 s20, s19, 2
	v_rcp_f32_e32 v32, v32
	v_rcp_f32_e32 v33, v33
	v_add_f32_e32 v24, 1.0, v24
	v_add_f32_e32 v22, v27, v95
	v_max_f32_e32 v27, 0xda24260, v20
	v_max_f32_e32 v35, 0xda24260, v21
	v_mov_b32_e32 v20, s20
	v_mov_b32_e32 v21, v3
	v_rcp_f32_e32 v24, v24
	v_mad_i64_i32 v[20:21], s[20:21], v134, 3, v[20:21]
	v_add_f32_e32 v28, v28, v84
	v_lshlrev_b64 v[20:21], 10, v[20:21]
	s_lshl_b32 s19, s19, 8
	v_mul_f32_e32 v28, 0xbfb8aa3b, v28
	s_and_b32 s34, s19, 0x300
	v_lshl_add_u64 v[20:21], s[46:47], 0, v[20:21]
	v_exp_f32_e32 v28, v28
	v_max_f32_e32 v32, 0xda24260, v32
	v_max_f32_e32 v33, 0xda24260, v33
	v_lshl_add_u64 v[20:21], v[20:21], 0, s[34:35]
	v_max_f32_e32 v39, 0xda24260, v24
	v_lshl_add_u64 v[24:25], v[20:21], 0, v[2:3]
	v_add_u32_e32 v20, 0xc4820000, v32
	v_add_u32_e32 v21, 0xc4820000, v33
	v_ashrrev_i32_e32 v20, 18, v20
	v_ashrrev_i32_e32 v21, 18, v21
	v_med3_i32 v20, v20, 0, v236
	v_med3_i32 v21, v21, 0, v236
	v_add_f32_e32 v28, 1.0, v28
	v_rcp_f32_e32 v28, v28
	v_lshl_or_b32 v20, v21, 8, v20
	v_add_u32_e32 v21, 0xc4820000, v26
	v_add_u32_e32 v26, 0xc4820000, v27
	v_ashrrev_i32_e32 v21, 18, v21
	v_ashrrev_i32_e32 v26, 18, v26
	v_med3_i32 v21, v21, 0, v236
	v_med3_i32 v26, v26, 0, v236
	v_max_f32_e32 v28, 0xda24260, v28
	v_lshlrev_b32_e32 v21, 16, v21
	v_lshlrev_b32_e32 v26, 24, v26
	v_or3_b32 v20, v20, v21, v26
	v_add_u32_e32 v21, 0xc4820000, v28
	v_add_u32_e32 v26, 0xc4820000, v29
	v_ashrrev_i32_e32 v21, 18, v21
	v_ashrrev_i32_e32 v26, 18, v26
	v_mul_f32_e32 v22, 0xbfb8aa3b, v22
	v_med3_i32 v21, v21, 0, v236
	v_med3_i32 v26, v26, 0, v236
	v_exp_f32_e32 v22, v22
	v_add_u32_e32 v27, 0xc4820000, v35
	v_lshl_or_b32 v21, v26, 8, v21
	v_add_u32_e32 v26, 0xc4820000, v30
	v_ashrrev_i32_e32 v26, 18, v26
	v_ashrrev_i32_e32 v27, 18, v27
	v_med3_i32 v26, v26, 0, v236
	v_med3_i32 v27, v27, 0, v236
	v_add_f32_e32 v22, 1.0, v22
	v_rcp_f32_e32 v22, v22
	v_lshlrev_b32_e32 v26, 16, v26
	v_lshlrev_b32_e32 v27, 24, v27
	v_or3_b32 v21, v21, v26, v27
	v_add_u32_e32 v26, 0xc4820000, v36
	v_add_u32_e32 v27, 0xc4820000, v34
	v_add_f32_e32 v23, v23, v99
	v_ashrrev_i32_e32 v26, 18, v26
	v_ashrrev_i32_e32 v27, 18, v27
	v_mul_f32_e32 v23, 0xbfb8aa3b, v23
	v_med3_i32 v26, v26, 0, v236
	v_med3_i32 v27, v27, 0, v236
	v_exp_f32_e32 v23, v23
	v_max_f32_e32 v22, 0xda24260, v22
	v_add_u32_e32 v22, 0xc4820000, v22
	v_lshl_or_b32 v26, v27, 8, v26
	v_add_u32_e32 v27, 0xc4820000, v39
	v_ashrrev_i32_e32 v27, 18, v27
	v_ashrrev_i32_e32 v22, 18, v22
	v_med3_i32 v27, v27, 0, v236
	v_med3_i32 v22, v22, 0, v236
	v_add_f32_e32 v23, 1.0, v23
	v_rcp_f32_e32 v23, v23
	v_lshlrev_b32_e32 v27, 16, v27
	v_lshlrev_b32_e32 v22, 24, v22
	v_or3_b32 v22, v26, v27, v22
	v_add_u32_e32 v26, 0xc4820000, v37
	v_add_u32_e32 v27, 0xc4820000, v38
	v_ashrrev_i32_e32 v26, 18, v26
	v_ashrrev_i32_e32 v27, 18, v27
	v_med3_i32 v26, v26, 0, v236
	v_med3_i32 v27, v27, 0, v236
	v_max_f32_e32 v23, 0xda24260, v23
	v_add_u32_e32 v23, 0xc4820000, v23
	v_lshl_or_b32 v26, v27, 8, v26
	v_add_u32_e32 v27, 0xc4820000, v31
	v_ashrrev_i32_e32 v27, 18, v27
	v_ashrrev_i32_e32 v23, 18, v23
	v_med3_i32 v27, v27, 0, v236
	v_med3_i32 v23, v23, 0, v236
	v_mov_b32_e32 v38, v54
	v_lshlrev_b32_e32 v27, 16, v27
	v_lshlrev_b32_e32 v23, 24, v23
	v_or3_b32 v23, v26, v27, v23
	global_store_dwordx4 v[24:25], v[20:23], off
	s_and_b64 vcc, exec, s[40:41]
	s_mov_b64 s[26:27], -1
	s_cbranch_vccz .LBB0_1050

.LBB0_891:
	s_waitcnt lgkmcnt(1)
	v_add_f32_e32 v8, v8, v76
	s_waitcnt lgkmcnt(0)
	v_add_f32_e32 v5, v5, v81
	v_mul_f32_e32 v8, 0xbfb8aa3b, v8
	v_add_f32_e32 v4, v4, v80
	v_mul_f32_e32 v5, 0xbfb8aa3b, v5
	v_exp_f32_e32 v8, v8
	v_mul_f32_e32 v4, 0xbfb8aa3b, v4
	v_exp_f32_e32 v5, v5
	v_exp_f32_e32 v4, v4
	v_add_f32_e32 v8, 1.0, v8
	v_add_f32_e32 v13, v13, v69
	v_add_f32_e32 v5, 1.0, v5
	v_rcp_f32_e32 v8, v8
	v_add_f32_e32 v4, 1.0, v4
	v_mul_f32_e32 v13, 0xbfb8aa3b, v13
	v_rcp_f32_e32 v5, v5
	v_rcp_f32_e32 v4, v4
	v_exp_f32_e32 v13, v13
	v_max_f32_e32 v20, 0xda24260, v8
	v_add_f32_e32 v8, v9, v77
	v_add_f32_e32 v9, v18, v74
	v_max_f32_e32 v22, 0xda24260, v5
	v_add_f32_e32 v5, v14, v70
	v_max_f32_e32 v21, 0xda24260, v4
	v_add_f32_e32 v4, 1.0, v13
	v_mul_f32_e32 v8, 0xbfb8aa3b, v8
	v_mul_f32_e32 v9, 0xbfb8aa3b, v9
	v_mul_f32_e32 v5, 0xbfb8aa3b, v5
	v_exp_f32_e32 v8, v8
	v_rcp_f32_e32 v4, v4
	v_exp_f32_e32 v9, v9
	v_exp_f32_e32 v5, v5
	v_add_f32_e32 v6, v6, v82
	v_add_f32_e32 v8, 1.0, v8
	v_max_f32_e32 v13, 0xda24260, v4
	v_add_f32_e32 v4, 1.0, v9
	v_add_f32_e32 v5, 1.0, v5
	v_mul_f32_e32 v6, 0xbfb8aa3b, v6
	v_rcp_f32_e32 v8, v8
	v_rcp_f32_e32 v4, v4
	v_rcp_f32_e32 v5, v5
	v_exp_f32_e32 v6, v6
	v_max_f32_e32 v18, 0xda24260, v8
	v_add_f32_e32 v8, v10, v78
	v_max_f32_e32 v10, 0xda24260, v4
	v_max_f32_e32 v14, 0xda24260, v5
	v_add_f32_e32 v4, 1.0, v6
	v_add_f32_e32 v5, v19, v75
	v_add_f32_e32 v6, v15, v71
	v_mul_f32_e32 v5, 0xbfb8aa3b, v5
	v_mul_f32_e32 v6, 0xbfb8aa3b, v6
	v_rcp_f32_e32 v4, v4
	v_exp_f32_e32 v5, v5
	v_exp_f32_e32 v6, v6
	v_add_f32_e32 v16, v16, v72
	v_add_f32_e32 v17, v17, v73
	v_mul_f32_e32 v16, 0xbfb8aa3b, v16
	v_mul_f32_e32 v17, 0xbfb8aa3b, v17
	v_exp_f32_e32 v16, v16
	v_exp_f32_e32 v17, v17
	v_mul_f32_e32 v8, 0xbfb8aa3b, v8
	v_max_f32_e32 v15, 0xda24260, v4
	v_add_f32_e32 v4, 1.0, v5
	v_add_f32_e32 v5, 1.0, v6
	v_exp_f32_e32 v8, v8
	v_rcp_f32_e32 v4, v4
	v_rcp_f32_e32 v5, v5
	s_add_i32 s87, s87, -11
	v_add_f32_e32 v16, 1.0, v16
	v_add_f32_e32 v17, 1.0, v17
	s_lshr_b32 s19, s87, 2
	v_rcp_f32_e32 v16, v16
	v_rcp_f32_e32 v17, v17
	v_add_f32_e32 v8, 1.0, v8
	v_add_f32_e32 v6, v11, v79
	v_max_f32_e32 v11, 0xda24260, v4
	v_max_f32_e32 v19, 0xda24260, v5
	v_mov_b32_e32 v4, s19
	v_mov_b32_e32 v5, v3
	v_rcp_f32_e32 v8, v8
	v_mad_i64_i32 v[4:5], s[20:21], v132, 3, v[4:5]
	v_add_f32_e32 v12, v12, v68
	v_lshlrev_b64 v[4:5], 10, v[4:5]
	s_lshl_b32 s19, s87, 8
	v_mul_f32_e32 v12, 0xbfb8aa3b, v12
	s_and_b32 s34, s19, 0x300
	v_lshl_add_u64 v[4:5], s[46:47], 0, v[4:5]
	v_exp_f32_e32 v12, v12
	v_max_f32_e32 v16, 0xda24260, v16
	v_max_f32_e32 v17, 0xda24260, v17
	v_lshl_add_u64 v[4:5], v[4:5], 0, s[34:35]
	v_max_f32_e32 v23, 0xda24260, v8
	v_lshl_add_u64 v[8:9], v[4:5], 0, v[2:3]
	v_add_u32_e32 v2, 0xc4820000, v16
	v_add_u32_e32 v4, 0xc4820000, v17
	v_ashrrev_i32_e32 v2, 18, v2
	v_ashrrev_i32_e32 v4, 18, v4
	v_med3_i32 v2, v2, 0, v236
	v_med3_i32 v4, v4, 0, v236
	v_add_f32_e32 v12, 1.0, v12
	v_rcp_f32_e32 v12, v12
	v_lshl_or_b32 v2, v4, 8, v2
	v_add_u32_e32 v4, 0xc4820000, v10
	v_add_u32_e32 v5, 0xc4820000, v11
	v_ashrrev_i32_e32 v4, 18, v4
	v_ashrrev_i32_e32 v5, 18, v5
	v_med3_i32 v4, v4, 0, v236
	v_med3_i32 v5, v5, 0, v236
	v_max_f32_e32 v12, 0xda24260, v12
	v_lshlrev_b32_e32 v4, 16, v4
	v_lshlrev_b32_e32 v5, 24, v5
	v_or3_b32 v4, v2, v4, v5
	v_add_u32_e32 v2, 0xc4820000, v12
	v_add_u32_e32 v5, 0xc4820000, v13
	v_ashrrev_i32_e32 v2, 18, v2
	v_ashrrev_i32_e32 v5, 18, v5
	v_mul_f32_e32 v6, 0xbfb8aa3b, v6
	v_med3_i32 v2, v2, 0, v236
	v_med3_i32 v5, v5, 0, v236
	v_exp_f32_e32 v6, v6
	v_add_u32_e32 v10, 0xc4820000, v19
	v_lshl_or_b32 v2, v5, 8, v2
	v_add_u32_e32 v5, 0xc4820000, v14
	v_ashrrev_i32_e32 v5, 18, v5
	v_ashrrev_i32_e32 v10, 18, v10
	v_med3_i32 v5, v5, 0, v236
	v_med3_i32 v10, v10, 0, v236
	v_add_f32_e32 v6, 1.0, v6
	v_rcp_f32_e32 v6, v6
	v_lshlrev_b32_e32 v5, 16, v5
	v_lshlrev_b32_e32 v10, 24, v10
	v_or3_b32 v5, v2, v5, v10
	v_add_u32_e32 v2, 0xc4820000, v20
	v_add_u32_e32 v10, 0xc4820000, v18
	v_add_f32_e32 v7, v7, v83
	v_ashrrev_i32_e32 v2, 18, v2
	v_ashrrev_i32_e32 v10, 18, v10
	v_mul_f32_e32 v7, 0xbfb8aa3b, v7
	v_med3_i32 v2, v2, 0, v236
	v_med3_i32 v10, v10, 0, v236
	v_exp_f32_e32 v7, v7
	v_max_f32_e32 v6, 0xda24260, v6
	v_add_u32_e32 v6, 0xc4820000, v6
	v_lshl_or_b32 v2, v10, 8, v2
	v_add_u32_e32 v10, 0xc4820000, v23
	v_ashrrev_i32_e32 v10, 18, v10
	v_ashrrev_i32_e32 v6, 18, v6
	v_med3_i32 v10, v10, 0, v236
	v_med3_i32 v6, v6, 0, v236
	v_add_f32_e32 v7, 1.0, v7
	v_rcp_f32_e32 v7, v7
	v_lshlrev_b32_e32 v10, 16, v10
	v_lshlrev_b32_e32 v6, 24, v6
	v_or3_b32 v6, v2, v10, v6
	v_add_u32_e32 v2, 0xc4820000, v21
	v_add_u32_e32 v10, 0xc4820000, v22
	v_ashrrev_i32_e32 v2, 18, v2
	v_ashrrev_i32_e32 v10, 18, v10
	v_med3_i32 v2, v2, 0, v236
	v_med3_i32 v10, v10, 0, v236
	v_max_f32_e32 v7, 0xda24260, v7
	v_add_u32_e32 v7, 0xc4820000, v7
	v_lshl_or_b32 v2, v10, 8, v2
	v_add_u32_e32 v10, 0xc4820000, v15
	v_ashrrev_i32_e32 v10, 18, v10
	v_ashrrev_i32_e32 v7, 18, v7
	v_med3_i32 v10, v10, 0, v236
	v_med3_i32 v7, v7, 0, v236
	v_mov_b32_e32 v28, v38
	v_lshlrev_b32_e32 v10, 16, v10
	v_lshlrev_b32_e32 v7, 24, v7
	v_or3_b32 v7, v2, v10, v7
	global_store_dwordx4 v[8:9], v[4:7], off
